# baseline (speedup 1.0000x reference)
.LBB3_10:
	s_or_b64 exec, exec, s[4:5]
	s_movk_i32 s4, 0x200
	v_cmp_gt_u32_e32 vcc, s4, v0
	s_waitcnt lgkmcnt(0)
	s_barrier
	s_and_saveexec_b64 s[22:23], vcc
	s_cbranch_execz .LBB3_13
	v_and_b32_e32 v1, 7, v0
	v_add_u32_e32 v15, 1, v1
	v_lshrrev_b32_e32 v5, 5, v0
	s_waitcnt vmcnt(0)
	v_min_u32_e32 v3, 7, v15
	v_add_u32_e32 v10, 1, v5
	v_lshlrev_b32_e32 v9, 2, v3
	v_add_u32_e32 v3, -1, v1
	v_min_u32_e32 v4, 7, v10
	v_mov_b32_e32 v7, 0x4650
	v_max_i32_e32 v13, 0, v3
	v_lshl_add_u32 v4, v4, 5, v7
	v_lshlrev_b32_e32 v6, 2, v1
	v_lshlrev_b32_e32 v18, 2, v13
	v_add_u32_e32 v11, v4, v9
	v_add_u32_e32 v12, v4, v6
	v_add_u32_e32 v13, v4, v18
	v_and_b32_e32 v4, 0xe0, v0
	v_add_u32_e32 v4, 0x4650, v4
	v_add_u32_e32 v14, v4, v9
	v_add_u32_e32 v16, v4, v6
	v_add_u32_e32 v17, v4, v18
	v_add_u32_e32 v4, -1, v5
	v_max_i32_e32 v19, 0, v4
	v_lshl_add_u32 v19, v19, 5, v7
	v_add_u32_e32 v7, v19, v9
	v_bfe_u32 v2, v0, 3, 2
	v_add_u32_e32 v9, v19, v6
	ds_read_b32 v11, v11
	ds_read_b32 v12, v12
	ds_read_b32 v13, v13
	ds_read_b32 v14, v14
	ds_read_b32 v16, v16
	ds_read_b32 v17, v17
	ds_read_b32 v20, v7
	ds_read_b32 v21, v9
	s_waitcnt lgkmcnt(7)
	v_lshrrev_b32_e32 v7, 2, v11
	s_mov_b32 s26, 0x3ffffffc
	v_and_or_b32 v7, v7, s26, v2
	v_lshlrev_b32_e32 v9, 2, v11
	v_mul_u32_u24_e32 v7, 60, v7
	v_and_b32_e32 v9, 60, v9
	v_add3_u32 v7, v9, v7, 4
	v_or_b32_e32 v9, v10, v15
	v_cmp_gt_u32_e32 vcc, 8, v9
	s_waitcnt lgkmcnt(6)
	v_lshrrev_b32_e32 v9, 2, v12
	v_and_or_b32 v9, v9, s26, v2
	v_lshlrev_b32_e32 v11, 2, v12
	v_mul_u32_u24_e32 v9, 60, v9
	v_and_b32_e32 v11, 60, v11
	v_add3_u32 v9, v11, v9, 8
	s_waitcnt lgkmcnt(5)
	v_lshrrev_b32_e32 v11, 2, v13
	v_and_or_b32 v11, v11, s26, v2
	v_lshlrev_b32_e32 v12, 2, v13
	v_mul_u32_u24_e32 v11, 60, v11
	v_and_b32_e32 v12, 60, v12
	v_or_b32_e32 v10, v10, v3
	v_cndmask_b32_e32 v7, 0, v7, vcc
	v_add3_u32 v11, v12, v11, 12
	v_cmp_gt_u32_e32 vcc, 8, v10
	s_waitcnt lgkmcnt(4)
	v_lshlrev_b32_e32 v12, 2, v14
	v_and_b32_e32 v12, 60, v12
	v_cndmask_b32_e32 v10, 0, v11, vcc
	v_lshrrev_b32_e32 v11, 2, v14
	v_and_or_b32 v11, v11, s26, v2
	v_mul_u32_u24_e32 v11, 60, v11
	s_movk_i32 s4, 0xf4
	v_add3_u32 v11, v11, v12, s4
	v_cmp_eq_u32_e32 vcc, 7, v1
	s_movk_i32 s4, 0xfc
	v_cmp_eq_u32_e64 s[6:7], 7, v5
	v_cndmask_b32_e64 v13, v11, 0, vcc
	s_waitcnt lgkmcnt(3)
	v_lshrrev_b32_e32 v11, 2, v16
	v_and_or_b32 v11, v11, s26, v2
	v_mul_u32_u24_e32 v12, 60, v11
	v_lshlrev_b32_e32 v11, 2, v16
	v_and_b32_e32 v14, 60, v11
	s_waitcnt lgkmcnt(2)
	v_lshrrev_b32_e32 v11, 2, v17
	v_and_or_b32 v11, v11, s26, v2
	v_lshlrev_b32_e32 v16, 2, v17
	v_mul_u32_u24_e32 v11, 60, v11
	v_and_b32_e32 v16, 60, v16
	v_add3_u32 v11, v11, v16, s4
	s_waitcnt lgkmcnt(1)
	v_lshrrev_b32_e32 v16, 2, v20
	v_and_or_b32 v16, v16, s26, v2
	v_lshlrev_b32_e32 v20, 2, v20
	v_cndmask_b32_e64 v9, v9, 0, s[6:7]
	v_cndmask_b32_e64 v17, 2, 1, s[6:7]
	v_mul_u32_u24_e32 v16, 60, v16
	v_and_b32_e32 v20, 60, v20
	s_movk_i32 s6, 0x1e4
	v_or_b32_e32 v15, v4, v15
	v_add3_u32 v16, v16, v20, s6
	v_cmp_gt_u32_e64 s[6:7], 8, v15
	s_waitcnt lgkmcnt(0)
	v_lshlrev_b32_e32 v20, 2, v21
	v_and_b32_e32 v20, 60, v20
	v_cndmask_b32_e64 v15, 0, v16, s[6:7]
	v_lshrrev_b32_e32 v16, 2, v21
	v_and_or_b32 v16, v16, s26, v2
	v_mul_u32_u24_e32 v16, 60, v16
	s_movk_i32 s6, 0x1e8
	v_add_u32_e32 v19, v19, v18
	v_cvt_f32_ubyte0_e32 v18, v2
	v_add3_u32 v16, v16, v20, s6
	v_add_f32_e32 v18, 0.5, v18
	v_mov_b32_e32 v20, -0.5
	v_fmamk_f32 v26, v18, 0x3e800000, v20
	v_cmp_gt_f32_e64 s[8:9], 0, v26
	v_sub_u32_e64 v20, v1, 1 clamp
	v_mov_b32_e32 v22, 0x4750
	v_subbrev_co_u32_e64 v18, s[12:13], 0, v5, s[8:9]
	v_cmp_ngt_f32_e64 s[12:13], 0, v26
	v_max_i32_e32 v18, 0, v18
	v_min_u32_e32 v21, 6, v1
	v_addc_co_u32_e64 v5, s[12:13], 0, v5, s[12:13]
	v_min_u32_e32 v5, 7, v5
	v_lshl_add_u32 v18, v18, 5, v22
	v_lshlrev_b32_e32 v20, 2, v20
	v_lshl_add_u32 v5, v5, 5, v22
	v_add_u32_e32 v23, v18, v20
	v_add_u32_e32 v22, v5, v20
	v_lshlrev_b32_e32 v20, 2, v21
	v_add_u32_e32 v24, v18, v6
	v_add_u32_e32 v6, v5, v6
	v_add_u32_e32 v25, v18, v20
	v_add_u32_e32 v5, v5, v20
	v_lshlrev_b32_e32 v18, 1, v7
	ds_read_b32 v19, v19
	ds_read_b32 v20, v23
	ds_read_b32 v22, v22
	ds_read_b32 v21, v24
	ds_read_b32 v23, v6
	ds_read_b32 v24, v25 offset:4
	ds_read_b32 v25, v5 offset:4
	ds_read_b64 v[6:7], v18
	s_waitcnt lgkmcnt(7)
	v_lshrrev_b32_e32 v5, 2, v19
	v_and_or_b32 v2, v5, s26, v2
	v_lshlrev_b32_e32 v5, 2, v19
	v_cmp_gt_u32_e64 s[6:7], 8, v4
	v_mul_u32_u24_e32 v2, 60, v2
	v_and_b32_e32 v5, 60, v5
	s_movk_i32 s12, 0x1ec
	v_cmp_gt_u32_e64 s[4:5], 8, v3
	v_cndmask_b32_e64 v16, 0, v16, s[6:7]
	v_add3_u32 v2, v2, v5, s12
	v_addc_co_u32_e64 v5, s[6:7], 0, v17, s[6:7]
	v_cndmask_b32_e64 v17, 2, 1, vcc
	v_addc_co_u32_e64 v17, vcc, 0, v17, s[4:5]
	v_mul_u32_u24_e32 v5, v5, v17
	v_cvt_f32_ubyte0_e32 v5, v5
	v_cndmask_b32_e64 v11, 0, v11, s[4:5]
	v_div_scale_f32 v17, s[4:5], v5, v5, 1.0
	v_rcp_f32_e32 v19, v17
	v_or_b32_e32 v3, v4, v3
	v_cmp_gt_u32_e32 vcc, 8, v3
	s_mov_b32 s4, 0x3ec00000
	s_mov_b32 s5, 0x3f600000
	v_cndmask_b32_e32 v30, 0, v2, vcc
	v_fma_f32 v2, -v17, v19, 1.0
	v_fmac_f32_e32 v19, v2, v19
	v_div_scale_f32 v2, vcc, 1.0, v5, 1.0
	v_mul_f32_e32 v3, v2, v19
	v_fma_f32 v4, -v17, v3, v2
	v_fmac_f32_e32 v3, v4, v19
	v_fma_f32 v2, -v17, v3, v2
	v_div_fmas_f32 v2, v2, v19, v3
	v_div_fixup_f32 v4, v2, v5, 1.0
	v_add_f32_e32 v2, 1.0, v26
	v_cndmask_b32_e64 v3, v26, v2, s[8:9]
	v_mov_b32_e32 v26, v3
	v_sub_f32_e32 v2, 1.0, v3
	s_waitcnt lgkmcnt(3)
	v_pk_mul_f32 v[22:23], v[26:27], v[22:23] op_sel_hi:[0,1]
	s_waitcnt lgkmcnt(1)
	v_pk_mul_f32 v[24:25], v[2:3], v[24:25]
	v_pk_fma_f32 v[2:3], v[2:3], v[20:21], v[22:23] op_sel_hi:[0,1,1]
	s_mov_b32 s7, 0x3f200000
	s_mov_b32 s6, 0x3e000000
	v_pk_mul_f32 v[20:21], v[2:3], s[4:5]
	v_pk_mul_f32 v[22:23], v[2:3], s[6:7]
	v_pk_add_f32 v[24:25], v[24:25], v[24:25] op_sel:[0,1] op_sel_hi:[0,1]
	v_pk_fma_f32 v[2:3], v[2:3], s[4:5], v[22:23] op_sel:[0,0,1] op_sel_hi:[1,1,0]
	s_mov_b32 s7, s4
	v_mov_b32_e32 v22, v21
	v_pk_fma_f32 v[20:21], v[24:25], s[6:7], v[22:23]
	s_lshr_b32 s4, s2, 2
	v_lshlrev_b32_e32 v22, 4, v1
	v_lshlrev_b32_e32 v1, 1, v9
	v_lshrrev_b32_e32 v8, 3, v0
	s_and_b32 s4, s4, 0xe0
	s_lshl_b32 s3, s3, 7
	ds_read_b64 v[24:25], v1
	v_or_b32_e32 v8, s4, v8
	s_and_b32 s26, s3, 0x380
	s_movk_i32 s3, 0xf0
	v_pk_mul_f32 v[2:3], v[4:5], v[2:3] op_sel_hi:[0,1]
	v_pk_mul_f32 v[4:5], v[4:5], v[20:21] op_sel_hi:[0,1]
	v_or_b32_e32 v20, s20, v8
	v_lshlrev_b32_e32 v8, 1, v10
	v_add3_u32 v9, v12, v14, s3
	v_lshlrev_b32_e32 v10, 1, v13
	v_lshlrev_b32_e32 v9, 1, v9
	ds_read_b64 v[12:13], v8
	ds_read_b64 v[26:27], v10
	ds_read_b64 v[28:29], v9 offset:16
	s_waitcnt lgkmcnt(3)
	v_pk_add_f16 v6, v6, v24
	v_pk_add_f16 v7, v7, v25
	s_waitcnt lgkmcnt(2)
	v_pk_add_f16 v6, v6, v12
	v_pk_add_f16 v7, v7, v13
	s_waitcnt lgkmcnt(1)
	v_pk_add_f16 v6, v6, v26
	v_pk_add_f16 v7, v7, v27
	v_lshlrev_b32_e32 v12, 1, v11
	s_waitcnt lgkmcnt(0)
	v_pk_add_f16 v19, v7, v29
	v_pk_add_f16 v23, v6, v28
	ds_read_b64 v[6:7], v12
	v_lshlrev_b32_e32 v13, 1, v15
	v_lshlrev_b32_e32 v14, 1, v16
	v_lshlrev_b32_e32 v11, 1, v30
	ds_read_b64 v[16:17], v13
	ds_read_b64 v[24:25], v14
	ds_read_b64 v[26:27], v11
	s_waitcnt lgkmcnt(3)
	v_pk_add_f16 v6, v23, v6
	v_pk_add_f16 v7, v19, v7
	s_load_dwordx2 s[24:25], s[0:1], 0x30
	s_waitcnt lgkmcnt(0)
	v_pk_add_f16 v7, v7, v17
	v_pk_add_f16 v6, v6, v16
	v_pk_add_f16 v7, v7, v25
	v_pk_add_f16 v6, v6, v24
	v_pk_add_f16 v7, v7, v27
	v_pk_add_f16 v6, v6, v26
	v_mov_b32_e32 v21, s21
	v_cvt_f32_f16_e32 v16, v6
	v_cvt_f32_f16_sdwa v17, v6 dst_sel:DWORD dst_unused:UNUSED_PAD src0_sel:WORD_1
	v_cvt_f32_f16_e32 v24, v7
	v_cvt_f32_f16_sdwa v25, v7 dst_sel:DWORD dst_unused:UNUSED_PAD src0_sel:WORD_1
	v_lshlrev_b64 v[20:21], 10, v[20:21]
	s_mov_b32 s27, 0
	v_lshl_add_u64 v[20:21], s[24:25], 0, v[20:21]
	v_lshl_add_u64 v[20:21], v[20:21], 0, s[26:27]
	v_mov_b32_e32 v23, 0
	s_movk_i32 s3, 0x100
	v_lshl_add_u64 v[6:7], v[20:21], 0, v[22:23]
	v_pk_mul_f32 v[20:21], v[2:3], v[16:17]
	v_pk_mul_f32 v[22:23], v[4:5], v[24:25]
	v_cmp_gt_u32_e32 vcc, s3, v0
	global_store_dwordx4 v[6:7], v[20:23], off nt
	s_and_b64 exec, exec, vcc
	s_cbranch_execz .LBB3_13
	ds_read_b64 v[16:17], v18 offset:7208
	ds_read_b64 v[18:19], v1 offset:7208
	ds_read_b64 v[20:21], v8 offset:7208
	ds_read_b64 v[22:23], v10 offset:7208
	v_add_co_u32_e32 v6, vcc, 0x40000, v6
	s_waitcnt lgkmcnt(2)
	v_pk_add_f16 v8, v17, v19
	v_pk_add_f16 v1, v16, v18
	s_waitcnt lgkmcnt(1)
	v_pk_add_f16 v10, v8, v21
	ds_read_b64 v[8:9], v9 offset:7224
	ds_read_b64 v[16:17], v12 offset:7208
	ds_read_b64 v[12:13], v13 offset:7208
	ds_read_b64 v[14:15], v14 offset:7208
	v_pk_add_f16 v1, v1, v20
	s_waitcnt lgkmcnt(4)
	v_pk_add_f16 v10, v10, v23
	v_pk_add_f16 v1, v1, v22
	s_waitcnt lgkmcnt(3)
	v_pk_add_f16 v9, v10, v9
	v_pk_add_f16 v1, v1, v8
	s_waitcnt lgkmcnt(2)
	v_pk_add_f16 v10, v9, v17
	ds_read_b64 v[8:9], v11 offset:7208
	v_pk_add_f16 v1, v1, v16
	s_waitcnt lgkmcnt(2)
	v_pk_add_f16 v10, v10, v13
	v_pk_add_f16 v1, v1, v12
	s_waitcnt lgkmcnt(1)
	v_pk_add_f16 v10, v10, v15
	v_pk_add_f16 v1, v1, v14
	s_waitcnt lgkmcnt(0)
	v_pk_add_f16 v11, v10, v9
	v_pk_add_f16 v1, v1, v8
	v_cvt_f32_f16_e32 v10, v11
	v_cvt_f32_f16_e32 v8, v1
	v_cvt_f32_f16_sdwa v9, v1 dst_sel:DWORD dst_unused:UNUSED_PAD src0_sel:WORD_1
	v_cvt_f32_f16_sdwa v11, v11 dst_sel:DWORD dst_unused:UNUSED_PAD src0_sel:WORD_1
	v_addc_co_u32_e32 v7, vcc, 0, v7, vcc
	v_pk_mul_f32 v[2:3], v[2:3], v[8:9]
	v_pk_mul_f32 v[4:5], v[4:5], v[10:11]
	global_store_dwordx4 v[6:7], v[2:5], off nt

.LBB3_19:
	s_or_b64 exec, exec, s[8:9]
	s_lshl_b32 s22, s3, 3
	s_and_b32 s8, s20, 64
	s_and_b32 s9, s22, 56
	s_or_b32 s8, s8, s9
	s_waitcnt lgkmcnt(0)
	s_lshl_b32 s6, s6, 1
	s_lshl_b32 s23, s8, 7
	s_ashr_i32 s9, s6, 31
	s_add_u32 s8, s6, s23
	s_addc_u32 s9, s9, 0
	s_lshl_b64 s[8:9], s[8:9], 8
	s_add_u32 s6, s4, s8
	s_addc_u32 s8, s5, s9
	s_lshl_b32 s4, s7, 1
	s_ashr_i32 s5, s4, 31
	v_mul_u32_u24_e32 v1, 0x1112, v0
	s_lshl_b64 s[4:5], s[4:5], 1
	v_lshrrev_b32_e32 v34, 16, v1
	s_add_u32 s6, s6, s4
	v_mad_i32_i24 v8, v34, -15, v0
	v_mov_b32_e32 v1, 0x1c00
	v_mov_b32_e32 v4, 0x1d00
	v_cmp_lt_u32_e32 vcc, 14, v0
	s_addc_u32 s7, s8, s5
	s_waitcnt vmcnt(0)
	v_lshlrev_b32_e32 v2, 1, v8
	v_cndmask_b32_e32 v4, v1, v4, vcc
	v_mov_b32_e32 v5, 0
	v_ashrrev_i32_e32 v3, 31, v2
	v_lshl_add_u64 v[6:7], s[6:7], 0, v[4:5]
	v_lshl_add_u64 v[6:7], v[2:3], 1, v[6:7]
	v_add_co_u32_e32 v6, vcc, 0x38000, v6
	s_movk_i32 s4, 0xff
	s_nop 0
	v_addc_co_u32_e32 v7, vcc, 0, v7, vcc
	global_load_dword v1, v[6:7], off
	v_lshlrev_b32_e32 v27, 2, v8
	v_cmp_gt_u32_e32 vcc, s4, v0
	v_mad_u32_u24 v26, v34, 60, v27
	s_and_saveexec_b64 s[4:5], vcc
	s_cbranch_execz .LBB3_21
	v_min_u32_e32 v4, 18, v34
	v_lshlrev_b32_e32 v4, 8, v4
	v_lshl_add_u64 v[8:9], s[6:7], 0, v[4:5]
	v_lshlrev_b64 v[6:7], 1, v[2:3]
	v_lshl_add_u64 v[2:3], v[8:9], 0, v[6:7]
	v_add_co_u32_e32 v2, vcc, 0x38000, v2
	v_add_u32_e32 v29, 0xcc, v34
	s_nop 0
	v_addc_co_u32_e32 v3, vcc, 0, v3, vcc
	v_min_u32_e32 v8, 0xef, v29
	global_load_dword v28, v[2:3], off offset:2816
	v_mul_lo_u16_e32 v2, 0x89, v8
	v_lshrrev_b16_e32 v9, 12, v2
	s_movk_i32 s8, 0xffe2
	v_mad_i32_i24 v8, v9, s8, v8
	v_lshlrev_b32_e32 v4, 15, v9
	v_ashrrev_i32_e32 v9, 31, v8
	v_lshl_add_u64 v[2:3], s[6:7], 0, v[4:5]
	v_lshlrev_b64 v[8:9], 8, v[8:9]
	v_lshl_add_u64 v[2:3], v[2:3], 0, v[8:9]
	v_add_u32_e32 v31, 0xbb, v34
	v_lshl_add_u64 v[2:3], v[2:3], 0, v[6:7]
	v_min_u32_e32 v8, 0xef, v31
	global_load_dword v30, v[2:3], off
	v_mul_lo_u16_e32 v2, 0x89, v8
	v_lshrrev_b16_e32 v9, 12, v2
	v_mad_i32_i24 v8, v9, s8, v8
	v_lshlrev_b32_e32 v4, 15, v9
	v_ashrrev_i32_e32 v9, 31, v8
	v_lshl_add_u64 v[2:3], s[6:7], 0, v[4:5]
	v_lshlrev_b64 v[8:9], 8, v[8:9]
	v_lshl_add_u64 v[2:3], v[2:3], 0, v[8:9]
	v_lshl_add_u64 v[2:3], v[2:3], 0, v[6:7]
	global_load_dword v32, v[2:3], off
	v_add_u32_e32 v2, 0xaa, v34
	v_mul_lo_u16_e32 v3, 0x89, v2
	v_lshrrev_b16_e32 v33, 12, v3
	v_mad_i32_i24 v2, v33, s8, v2
	v_lshlrev_b32_e32 v4, 15, v33
	v_ashrrev_i32_e32 v3, 31, v2
	v_lshl_add_u64 v[8:9], s[6:7], 0, v[4:5]
	v_lshlrev_b64 v[10:11], 8, v[2:3]
	v_lshl_add_u64 v[8:9], v[8:9], 0, v[10:11]
	v_lshl_add_u64 v[8:9], v[8:9], 0, v[6:7]
	global_load_dword v3, v[8:9], off
	v_add_u32_e32 v8, 0x99, v34
	v_mul_lo_u16_e32 v4, 0x89, v8
	v_lshrrev_b16_e32 v35, 12, v4
	v_mad_i32_i24 v8, v35, s8, v8
	v_lshlrev_b32_e32 v4, 15, v35
	v_ashrrev_i32_e32 v9, 31, v8
	v_lshl_add_u64 v[10:11], s[6:7], 0, v[4:5]
	v_lshlrev_b64 v[12:13], 8, v[8:9]
	v_lshl_add_u64 v[10:11], v[10:11], 0, v[12:13]
	v_lshl_add_u64 v[10:11], v[10:11], 0, v[6:7]
	global_load_dword v9, v[10:11], off
	v_add_u32_e32 v10, 0x88, v34
	v_mul_lo_u16_e32 v4, 0x89, v10
	v_lshrrev_b16_e32 v36, 12, v4
	v_mad_i32_i24 v10, v36, s8, v10
	v_lshlrev_b32_e32 v4, 15, v36
	v_ashrrev_i32_e32 v11, 31, v10
	v_lshl_add_u64 v[12:13], s[6:7], 0, v[4:5]
	v_lshlrev_b64 v[14:15], 8, v[10:11]
	v_lshl_add_u64 v[12:13], v[12:13], 0, v[14:15]
	v_lshl_add_u64 v[12:13], v[12:13], 0, v[6:7]
	global_load_dword v11, v[12:13], off
	v_add_u32_e32 v12, 0x77, v34
	v_mul_lo_u16_e32 v4, 0x89, v12
	v_lshrrev_b16_e32 v37, 12, v4
	v_mad_i32_i24 v12, v37, s8, v12
	v_lshlrev_b32_e32 v4, 15, v37
	v_ashrrev_i32_e32 v13, 31, v12
	v_lshl_add_u64 v[14:15], s[6:7], 0, v[4:5]
	v_lshlrev_b64 v[16:17], 8, v[12:13]
	v_lshl_add_u64 v[14:15], v[14:15], 0, v[16:17]
	v_lshl_add_u64 v[14:15], v[14:15], 0, v[6:7]
	global_load_dword v13, v[14:15], off
	v_add_u32_e32 v14, 0x66, v34
	v_mul_lo_u16_e32 v4, 0x89, v14
	v_lshrrev_b16_e32 v38, 12, v4
	v_mad_i32_i24 v14, v38, s8, v14
	v_lshlrev_b32_e32 v4, 15, v38
	v_ashrrev_i32_e32 v15, 31, v14
	v_lshl_add_u64 v[16:17], s[6:7], 0, v[4:5]
	v_lshlrev_b64 v[18:19], 8, v[14:15]
	v_lshl_add_u64 v[16:17], v[16:17], 0, v[18:19]
	v_lshl_add_u64 v[16:17], v[16:17], 0, v[6:7]
	global_load_dword v15, v[16:17], off
	v_add_u32_e32 v16, 0x55, v34
	v_mul_lo_u16_e32 v4, 0x89, v16
	v_lshrrev_b16_e32 v39, 12, v4
	v_mad_i32_i24 v16, v39, s8, v16
	v_lshlrev_b32_e32 v4, 15, v39
	v_ashrrev_i32_e32 v17, 31, v16
	v_lshl_add_u64 v[18:19], s[6:7], 0, v[4:5]
	v_lshlrev_b64 v[20:21], 8, v[16:17]
	v_lshl_add_u64 v[18:19], v[18:19], 0, v[20:21]
	v_lshl_add_u64 v[18:19], v[18:19], 0, v[6:7]
	global_load_dword v17, v[18:19], off
	v_add_u32_e32 v18, 0x44, v34
	v_mul_lo_u16_e32 v4, 0x89, v18
	v_lshrrev_b16_e32 v40, 12, v4
	v_mad_i32_i24 v18, v40, s8, v18
	v_lshlrev_b32_e32 v4, 15, v40
	v_ashrrev_i32_e32 v19, 31, v18
	v_lshl_add_u64 v[20:21], s[6:7], 0, v[4:5]
	v_lshlrev_b64 v[22:23], 8, v[18:19]
	v_lshl_add_u64 v[20:21], v[20:21], 0, v[22:23]
	v_lshl_add_u64 v[20:21], v[20:21], 0, v[6:7]
	global_load_dword v19, v[20:21], off
	v_add_u32_e32 v20, 51, v34
	v_mul_lo_u16_e32 v4, 0x89, v20
	v_lshrrev_b16_e32 v41, 12, v4
	v_mad_i32_i24 v20, v41, s8, v20
	v_lshlrev_b32_e32 v4, 15, v41
	v_ashrrev_i32_e32 v21, 31, v20
	v_lshl_add_u64 v[22:23], s[6:7], 0, v[4:5]
	v_lshlrev_b64 v[24:25], 8, v[20:21]
	v_lshl_add_u64 v[22:23], v[22:23], 0, v[24:25]
	v_lshl_add_u64 v[22:23], v[22:23], 0, v[6:7]
	global_load_dword v21, v[22:23], off
	v_add_u32_e32 v22, 34, v34
	v_mul_lo_u16_e32 v4, 0x89, v22
	v_lshrrev_b16_e32 v42, 12, v4
	v_mad_i32_i24 v22, v42, s8, v22
	v_lshlrev_b32_e32 v4, 15, v42
	v_ashrrev_i32_e32 v23, 31, v22
	v_lshl_add_u64 v[24:25], s[6:7], 0, v[4:5]
	v_lshlrev_b64 v[44:45], 8, v[22:23]
	v_lshl_add_u64 v[24:25], v[24:25], 0, v[44:45]
	v_lshl_add_u64 v[24:25], v[24:25], 0, v[6:7]
	global_load_dword v23, v[24:25], off
	v_add_u32_e32 v24, 17, v34
	v_mul_lo_u16_e32 v4, 0x89, v24
	v_lshrrev_b16_e32 v43, 12, v4
	v_mad_i32_i24 v24, v43, s8, v24
	s_movk_i32 s9, 0x89
	v_lshlrev_b32_e32 v4, 15, v43
	v_ashrrev_i32_e32 v25, 31, v24
	v_lshl_add_u64 v[44:45], s[6:7], 0, v[4:5]
	v_lshlrev_b64 v[46:47], 8, v[24:25]
	v_mul_lo_u16_sdwa v4, v34, s9 dst_sel:DWORD dst_unused:UNUSED_PAD src0_sel:BYTE_0 src1_sel:DWORD
	v_lshl_add_u64 v[44:45], v[44:45], 0, v[46:47]
	v_lshrrev_b16_e32 v48, 12, v4
	v_lshl_add_u64 v[44:45], v[44:45], 0, v[6:7]
	v_lshlrev_b32_e32 v4, 15, v48
	global_load_dword v25, v[44:45], off
	v_lshl_add_u64 v[44:45], s[6:7], 0, v[4:5]
	v_mad_i32_i24 v4, v48, s8, v34
	v_ashrrev_i32_e32 v5, 31, v4
	v_lshlrev_b64 v[46:47], 8, v[4:5]
	v_lshl_add_u64 v[44:45], v[44:45], 0, v[46:47]
	v_lshl_add_u64 v[6:7], v[44:45], 0, v[6:7]
	global_load_dword v5, v[6:7], off
	v_mul_u32_u24_e32 v6, 0x70c, v48
	v_mul_u32_u24_e32 v4, 60, v4
	v_add3_u32 v4, v6, v4, v27
	v_mul_u32_u24_e32 v2, 60, v2
	s_waitcnt vmcnt(0)
	ds_write_b32 v4, v5 offset:4
	v_mul_u32_u24_e32 v4, 0x70c, v43
	v_mul_u32_u24_e32 v5, 60, v24
	v_add3_u32 v4, v4, v5, v27
	ds_write_b32 v4, v25 offset:4
	v_mul_u32_u24_e32 v4, 0x70c, v42
	v_mul_u32_u24_e32 v5, 60, v22
	v_add3_u32 v4, v4, v5, v27
	ds_write_b32 v4, v23 offset:4
	v_mul_u32_u24_e32 v4, 0x70c, v41
	v_mul_u32_u24_e32 v5, 60, v20
	v_add3_u32 v4, v4, v5, v27
	ds_write_b32 v4, v21 offset:4
	v_mul_u32_u24_e32 v4, 0x70c, v40
	v_mul_u32_u24_e32 v5, 60, v18
	v_add3_u32 v4, v4, v5, v27
	ds_write_b32 v4, v19 offset:4
	v_mul_u32_u24_e32 v4, 0x70c, v39
	v_mul_u32_u24_e32 v5, 60, v16
	v_add3_u32 v4, v4, v5, v27
	ds_write_b32 v4, v17 offset:4
	v_mul_u32_u24_e32 v4, 0x70c, v38
	v_mul_u32_u24_e32 v5, 60, v14
	v_add3_u32 v4, v4, v5, v27
	ds_write_b32 v4, v15 offset:4
	v_mul_u32_u24_e32 v4, 0x70c, v37
	v_mul_u32_u24_e32 v5, 60, v12
	v_add3_u32 v4, v4, v5, v27
	ds_write_b32 v4, v13 offset:4
	v_mul_u32_u24_e32 v4, 0x70c, v36
	v_mul_u32_u24_e32 v5, 60, v10
	v_add3_u32 v4, v4, v5, v27
	ds_write_b32 v4, v11 offset:4
	v_mul_u32_u24_e32 v4, 0x70c, v35
	v_mul_u32_u24_e32 v5, 60, v8
	v_add3_u32 v4, v4, v5, v27
	ds_write_b32 v4, v9 offset:4
	v_mul_u32_u24_e32 v4, 0x70c, v33
	v_add3_u32 v2, v4, v2, v27
	ds_write_b32 v2, v3 offset:4
	v_mul_lo_u16_e32 v2, 0x89, v31
	v_lshrrev_b16_e32 v2, 12, v2
	v_mad_i32_i24 v3, v2, s8, v31
	v_mul_u32_u24_e32 v2, 0x70c, v2
	v_mul_u32_u24_e32 v3, 60, v3
	v_add3_u32 v2, v2, v3, v27
	ds_write_b32 v2, v32 offset:4
	v_mul_lo_u16_e32 v2, 0x89, v29
	v_lshrrev_b16_e32 v2, 12, v2
	v_mad_i32_i24 v3, v2, s8, v29
	v_mul_u32_u24_e32 v2, 0x70c, v2
	v_mul_u32_u24_e32 v3, 60, v3
	v_add3_u32 v2, v2, v3, v27
	ds_write_b32 v2, v30 offset:4
	ds_write_b32 v26, v28 offset:13292

.LBB3_23:
	s_or_b64 exec, exec, s[4:5]
	v_and_b32_e32 v6, 7, v0
	s_waitcnt vmcnt(0)
	v_lshrrev_b32_e32 v1, 3, v0
	v_add_u32_e32 v15, 1, v6
	v_bfe_u32 v3, v1, 1, 3
	v_min_u32_e32 v2, 7, v15
	v_add_u32_e32 v9, 1, v3
	v_lshlrev_b32_e32 v11, 2, v2
	v_add_u32_e32 v2, -1, v6
	v_min_u32_e32 v4, 7, v9
	v_mov_b32_e32 v5, 0x4650
	v_max_i32_e32 v10, 0, v2
	v_lshl_add_u32 v8, v4, 5, v5
	v_lshlrev_b32_e32 v4, 2, v6
	v_lshlrev_b32_e32 v17, 2, v10
	v_lshl_add_u32 v10, v3, 5, v5
	v_add_u32_e32 v14, v10, v11
	v_add_u32_e32 v16, v10, v4
	v_add_u32_e32 v18, v10, v17
	v_add_u32_e32 v10, -1, v3
	v_max_i32_e32 v19, 0, v10
	v_lshl_add_u32 v19, v19, 5, v5
	v_add_u32_e32 v12, v8, v11
	v_add_u32_e32 v13, v8, v4
	v_add_u32_e32 v8, v8, v17
	v_add_u32_e32 v5, v19, v11
	s_waitcnt lgkmcnt(0)
	s_barrier
	v_bfe_u32 v1, v0, 3, 1
	v_add_u32_e32 v11, v19, v4
	ds_read_b32 v12, v12
	ds_read_b32 v13, v13
	ds_read_b32 v20, v8
	ds_read_b32 v14, v14
	ds_read_b32 v8, v16
	ds_read_b32 v16, v18
	ds_read_b32 v18, v5
	ds_read_b32 v21, v11
	s_waitcnt lgkmcnt(7)
	v_ashrrev_i32_e32 v5, 3, v12
	s_mov_b32 s24, 0x7ffffffe
	v_and_or_b32 v5, v5, s24, v1
	v_lshlrev_b32_e32 v11, 1, v12
	v_mul_u32_u24_e32 v5, 30, v5
	v_and_b32_e32 v11, 30, v11
	v_add3_u32 v5, v11, v5, 2
	v_or_b32_e32 v11, v9, v15
	v_cmp_gt_u32_e32 vcc, 8, v11
	s_waitcnt lgkmcnt(6)
	v_ashrrev_i32_e32 v11, 3, v13
	v_and_or_b32 v11, v11, s24, v1
	v_lshlrev_b32_e32 v12, 1, v13
	v_mul_u32_u24_e32 v11, 30, v11
	v_and_b32_e32 v12, 30, v12
	v_add3_u32 v11, v12, v11, 4
	s_waitcnt lgkmcnt(5)
	v_ashrrev_i32_e32 v12, 3, v20
	v_and_or_b32 v12, v12, s24, v1
	v_lshlrev_b32_e32 v13, 1, v20
	v_mul_u32_u24_e32 v12, 30, v12
	v_and_b32_e32 v13, 30, v13
	v_or_b32_e32 v9, v9, v2
	v_cndmask_b32_e32 v5, 0, v5, vcc
	v_add3_u32 v12, v13, v12, 6
	v_cmp_gt_u32_e32 vcc, 8, v9
	s_waitcnt lgkmcnt(4)
	v_ashrrev_i32_e32 v9, 3, v14
	v_lshlrev_b32_e32 v13, 1, v14
	s_waitcnt lgkmcnt(2)
	v_ashrrev_i32_e32 v14, 3, v16
	v_and_or_b32 v14, v14, s24, v1
	v_lshlrev_b32_e32 v16, 1, v16
	v_mul_u32_u24_e32 v14, 30, v14
	v_and_b32_e32 v16, 30, v16
	s_movk_i32 s6, 0x42
	v_add3_u32 v14, v14, v16, s6
	s_waitcnt lgkmcnt(1)
	v_ashrrev_i32_e32 v16, 3, v18
	v_cmp_eq_u32_e64 s[4:5], 7, v3
	v_and_or_b32 v16, v16, s24, v1
	v_lshlrev_b32_e32 v18, 1, v18
	v_cndmask_b32_e64 v11, v11, 0, s[4:5]
	v_cndmask_b32_e64 v24, 2, 1, s[4:5]
	v_mul_u32_u24_e32 v16, 30, v16
	v_and_b32_e32 v18, 30, v18
	s_movk_i32 s4, 0x7a
	v_or_b32_e32 v15, v10, v15
	v_add3_u32 v16, v16, v18, s4
	v_cmp_gt_u32_e64 s[4:5], 8, v15
	s_waitcnt lgkmcnt(0)
	v_lshlrev_b32_e32 v18, 1, v21
	v_and_b32_e32 v18, 30, v18
	v_cndmask_b32_e64 v15, 0, v16, s[4:5]
	v_ashrrev_i32_e32 v16, 3, v21
	v_and_or_b32 v16, v16, s24, v1
	v_mul_u32_u24_e32 v16, 30, v16
	s_movk_i32 s4, 0x7c
	v_add3_u32 v16, v16, v18, s4
	v_cvt_f32_ubyte0_e32 v18, v1
	v_add_f32_e32 v18, 0.5, v18
	v_fma_f32 v25, v18, 0.5, -0.5
	v_cmp_gt_f32_e64 s[8:9], 0, v25
	v_add_u32_e32 v17, v19, v17
	v_sub_u32_e64 v19, v6, 1 clamp
	v_subbrev_co_u32_e64 v18, s[10:11], 0, v3, s[8:9]
	v_cmp_ngt_f32_e64 s[10:11], 0, v25
	v_max_i32_e32 v18, 0, v18
	v_min_u32_e32 v20, 6, v6
	v_addc_co_u32_e64 v3, s[10:11], 0, v3, s[10:11]
	v_min_u32_e32 v3, 7, v3
	v_mov_b32_e32 v21, 0x4750
	v_lshl_add_u32 v18, v18, 5, v21
	v_lshlrev_b32_e32 v19, 2, v19
	v_lshl_add_u32 v3, v3, 5, v21
	v_lshlrev_b32_e32 v20, 2, v20
	v_add_u32_e32 v22, v18, v19
	v_add_u32_e32 v19, v3, v19
	v_add_u32_e32 v21, v18, v4
	v_add_u32_e32 v4, v3, v4
	v_add_u32_e32 v3, v3, v20
	v_and_or_b32 v9, v9, s24, v1
	v_add_u32_e32 v26, v18, v20
	ds_read_b32 v17, v17
	ds_read_b32 v18, v22
	ds_read_b32 v20, v19
	ds_read_b32 v22, v21
	ds_read_b32 v23, v4
	ds_read_b32 v19, v26 offset:4
	ds_read_b32 v21, v3 offset:4
	s_waitcnt lgkmcnt(6)
	v_ashrrev_i32_e32 v3, 3, v17
	v_cndmask_b32_e32 v12, 0, v12, vcc
	v_mul_u32_u24_e32 v9, 30, v9
	v_and_b32_e32 v13, 30, v13
	v_cmp_eq_u32_e32 vcc, 7, v6
	v_and_or_b32 v3, v3, s24, v1
	v_lshlrev_b32_e32 v4, 1, v17
	v_add3_u32 v9, v9, v13, 62
	v_cmp_gt_u32_e64 s[6:7], 8, v2
	v_cmp_gt_u32_e64 s[4:5], 8, v10
	v_mul_u32_u24_e32 v3, 30, v3
	v_and_b32_e32 v4, 30, v4
	s_movk_i32 s10, 0x7e
	v_cndmask_b32_e64 v17, 2, 1, vcc
	v_cndmask_b32_e64 v13, v9, 0, vcc
	v_cndmask_b32_e64 v16, 0, v16, s[4:5]
	v_add3_u32 v3, v3, v4, s10
	v_addc_co_u32_e64 v4, s[4:5], 0, v24, s[4:5]
	v_addc_co_u32_e64 v17, vcc, 0, v17, s[6:7]
	v_mul_u32_u24_e32 v4, v4, v17
	v_cvt_f32_ubyte0_e32 v4, v4
	v_div_scale_f32 v17, s[4:5], v4, v4, 1.0
	v_rcp_f32_e32 v24, v17
	v_or_b32_e32 v2, v10, v2
	v_cmp_gt_u32_e32 vcc, 8, v2
	s_load_dwordx2 s[12:13], s[0:1], 0x38
	v_fma_f32 v2, -v17, v24, 1.0
	v_cndmask_b32_e32 v26, 0, v3, vcc
	v_fmac_f32_e32 v24, v2, v24
	v_div_scale_f32 v2, vcc, 1.0, v4, 1.0
	v_mul_f32_e32 v3, v2, v24
	v_fma_f32 v10, -v17, v3, v2
	v_fmac_f32_e32 v3, v10, v24
	v_fma_f32 v2, -v17, v3, v2
	v_div_fmas_f32 v2, v2, v24, v3
	v_add_f32_e32 v3, 1.0, v25
	v_cndmask_b32_e64 v25, v25, v3, s[8:9]
	v_sub_f32_e32 v24, 1.0, v25
	s_waitcnt lgkmcnt(0)
	v_pk_mul_f32 v[22:23], v[24:25], v[22:23]
	v_mov_b32_e32 v10, v25
	v_add_f32_e32 v3, v22, v23
	v_pk_mul_f32 v[20:21], v[10:11], v[20:21] op_sel_hi:[0,1]
	v_div_fixup_f32 v2, v2, v4, 1.0
	v_mul_f32_e32 v4, 0x3f400000, v3
	v_pk_fma_f32 v[18:19], v[24:25], v[18:19], v[20:21] op_sel_hi:[0,1,1]
	s_mov_b32 s4, 0x3e800000
	v_pk_fma_f32 v[18:19], v[18:19], s[4:5], v[4:5] op_sel_hi:[1,0,0]
	v_cndmask_b32_e64 v14, 0, v14, s[6:7]
	v_pk_mul_f32 v[2:3], v[2:3], v[18:19] op_sel_hi:[0,1]
	s_lshr_b32 s4, s2, 2
	v_lshrrev_b32_e32 v19, 7, v0
	v_bfe_u32 v7, v0, 3, 4
	s_mov_b32 s21, 0
	v_ashrrev_i32_e32 v9, 3, v8
	s_and_b32 s8, s4, 0x70
	v_xor_b32_e32 v18, 7, v19
	s_mov_b64 s[6:7], 0
	v_lshlrev_b32_e32 v10, 1, v5
	v_lshlrev_b32_e32 v11, 1, v11
	v_lshlrev_b32_e32 v12, 1, v12
	v_lshlrev_b32_e32 v13, 1, v13
	v_lshlrev_b32_e32 v14, 1, v14
	v_lshlrev_b32_e32 v15, 1, v15
	v_lshlrev_b32_e32 v16, 1, v16
	v_lshlrev_b32_e32 v17, 1, v26
	s_and_saveexec_b64 s[4:5], s[6:7]
	s_cbranch_execz .LBB3_25
	s_mov_b32 s6, 0x3ffffffe
	v_and_or_b32 v4, v9, s6, v1
	s_or_b32 s6, s8, s23
	v_mul_u32_u24_e32 v22, 60, v4
	v_or_b32_e32 v4, s6, v7
	v_lshlrev_b32_e32 v4, 9, v4
	v_mov_b32_e32 v5, 0
	s_lshl_b32 s6, s20, 6
	v_lshlrev_b32_e32 v23, 2, v8
	v_lshl_add_u64 v[20:21], s[12:13], 0, v[4:5]
	s_and_b32 s20, s6, 0x1c0
	s_movk_i32 s6, 0x70c
	v_mul_u32_u24_e32 v4, 0x70c, v19
	v_and_b32_e32 v23, 60, v23
	v_add3_u32 v4, v4, v23, v22
	v_mad_u32_u24 v22, v19, s6, v10
	v_mad_u32_u24 v23, v19, s6, v11
	v_mad_u32_u24 v24, v19, s6, v12
	v_mad_u32_u24 v25, v19, s6, v13
	v_mad_u32_u24 v26, v19, s6, v14
	v_mad_u32_u24 v27, v19, s6, v15
	v_mad_u32_u24 v28, v19, s6, v16
	ds_read_b32 v22, v22
	ds_read_b32 v23, v23
	ds_read_b32 v24, v24
	ds_read_b32 v25, v25
	ds_read_b32 v26, v26
	ds_read_b32 v27, v27
	ds_read_b32 v28, v28
	ds_read_b32 v4, v4 offset:128
	s_waitcnt lgkmcnt(6)
	v_pk_add_f16 v22, v22, v23
	v_mad_u32_u24 v23, v19, s6, v17
	s_waitcnt lgkmcnt(5)
	v_pk_add_f16 v22, v22, v24
	ds_read_b32 v23, v23
	s_waitcnt lgkmcnt(5)
	v_pk_add_f16 v22, v22, v25
	v_lshl_add_u64 v[20:21], v[20:21], 0, s[20:21]
	s_waitcnt lgkmcnt(1)
	v_pk_add_f16 v4, v22, v4
	s_nop 0
	v_pk_add_f16 v4, v4, v26
	s_nop 0
	v_pk_add_f16 v4, v4, v27
	s_nop 0
	v_pk_add_f16 v4, v4, v28
	s_waitcnt lgkmcnt(0)
	v_pk_add_f16 v4, v4, v23
	s_nop 0
	v_cvt_f32_f16_e32 v22, v4
	v_cvt_f32_f16_sdwa v23, v4 dst_sel:DWORD dst_unused:UNUSED_PAD src0_sel:WORD_1
	v_lshlrev_b32_e32 v4, 3, v6
	v_lshl_add_u64 v[20:21], v[20:21], 0, v[4:5]
	v_lshlrev_b32_e32 v4, 16, v19
	v_pk_mul_f32 v[22:23], v[2:3], v[22:23]
	v_lshl_add_u64 v[4:5], v[20:21], 0, v[4:5]
	v_or_b32_e32 v19, 2, v19
	global_store_dwordx2 v[4:5], v[22:23], off nt
